# baseline (speedup 1.0000x reference)
	.text
	.protected	_Z7k_layerILi1EEvPKDF16_S1_PKfS3_S3_S3_S3_S3_S1_S1_S1_S1_S3_S3_PKhS5_PDF16_S6_PfS7_
	.globl	_Z7k_layerILi1EEvPKDF16_S1_PKfS3_S3_S3_S3_S3_S1_S1_S1_S1_S3_S3_PKhS5_PDF16_S6_PfS7_
	.p2align	8
	.type	_Z7k_layerILi1EEvPKDF16_S1_PKfS3_S3_S3_S3_S3_S1_S1_S1_S1_S3_S3_PKhS5_PDF16_S6_PfS7_,@function

.LBB2_17:
	s_and_b64 vcc, exec, s[2:3]
	s_cbranch_vccz .LBB2_27
	s_load_dwordx2 s[2:3], s[0:1], 0x70
	s_setprio 2
	s_load_dwordx4 s[4:7], s[0:1], 0x40
	s_lshr_b32 s11, s15, 7
	s_lshl_b32 s8, s12, 3
	s_or_b32 s8, s11, s8
	s_ashr_i32 s9, s8, 31
	s_bfe_u32 s10, s15, 0x10006
	s_lshl_b64 s[12:13], s[8:9], 12
	v_and_b32_e32 v156, 63, v0
	s_waitcnt lgkmcnt(0)
	s_add_u32 s12, s2, s12
	s_addc_u32 s13, s3, s13
	v_lshlrev_b32_e32 v1, 3, v156
	global_load_dwordx2 v[154:155], v1, s[12:13]
	global_load_dwordx2 v[150:151], v1, s[12:13] offset:512
	global_load_dwordx2 v[146:147], v1, s[12:13] offset:1024
	global_load_dwordx2 v[142:143], v1, s[12:13] offset:1536
	global_load_dwordx2 v[152:153], v1, s[12:13] offset:2048
	global_load_dwordx2 v[148:149], v1, s[12:13] offset:2560
	global_load_dwordx2 v[144:145], v1, s[12:13] offset:3072
	global_load_dwordx2 v[140:141], v1, s[12:13] offset:3584
	s_lshl_b32 s9, s14, 10
	s_lshl_b32 s12, s10, 9
	s_or_b32 s9, s12, s9
	v_or_b32_e32 v1, s9, v156
	v_lshlrev_b32_e32 v2, 4, v1
	v_mov_b32_e32 v3, 0
	v_lshl_add_u64 v[4:5], s[4:5], 0, v[2:3]
	s_movk_i32 s9, 0x1000
	v_add_co_u32_e32 v4, vcc, s9, v4
	v_lshlrev_b32_e32 v1, 2, v0
	s_nop 0
	v_addc_co_u32_e32 v5, vcc, 0, v5, vcc
	global_load_dwordx4 v[86:89], v[4:5], off
	global_load_dwordx4 v[78:81], v[4:5], off offset:1024
	global_load_dwordx4 v[70:73], v[4:5], off offset:2048
	global_load_dwordx4 v[66:69], v[4:5], off offset:3072
	global_load_dwordx4 v[122:125], v2, s[4:5]
	global_load_dwordx4 v[126:129], v2, s[6:7]
	global_load_dwordx4 v[114:117], v2, s[4:5] offset:1024
	global_load_dwordx4 v[118:121], v2, s[6:7] offset:1024
	global_load_dwordx4 v[106:109], v2, s[4:5] offset:2048
	global_load_dwordx4 v[110:113], v2, s[6:7] offset:2048
	global_load_dwordx4 v[98:101], v2, s[4:5] offset:3072
	global_load_dwordx4 v[102:105], v2, s[6:7] offset:3072
	v_lshl_add_u64 v[4:5], s[6:7], 0, v[2:3]
	v_add_co_u32_e32 v2, vcc, 0x1000, v4
	s_nop 1
	v_addc_co_u32_e32 v3, vcc, 0, v5, vcc
	global_load_dwordx4 v[94:97], v[2:3], off
	global_load_dwordx4 v[90:93], v[2:3], off offset:1024
	global_load_dwordx4 v[82:85], v[2:3], off offset:2048
	global_load_dwordx4 v[74:77], v[2:3], off offset:3072
	v_cmp_gt_u32_e32 vcc, 64, v0
	s_and_saveexec_b64 s[4:5], vcc
	s_cbranch_execz .LBB2_20
	s_load_dwordx2 s[0:1], s[0:1], 0x60
	v_lshl_or_b32 v2, s14, 8, v1
	v_add_u32_e32 v3, 0x1ee00, v1
	s_waitcnt lgkmcnt(0)
	global_load_dword v2, v2, s[0:1]
	s_waitcnt vmcnt(0)
	ds_write_b32 v3, v2

	.amdhsa_kernel _Z7k_layerILi1EEvPKDF16_S1_PKfS3_S3_S3_S3_S3_S1_S1_S1_S1_S3_S3_PKhS5_PDF16_S6_PfS7_
		.amdhsa_group_segment_fixed_size 126720
		.amdhsa_private_segment_fixed_size 0
		.amdhsa_kernarg_size 160
		.amdhsa_user_sgpr_count 2
		.amdhsa_user_sgpr_dispatch_ptr 0
		.amdhsa_user_sgpr_queue_ptr 0
		.amdhsa_user_sgpr_kernarg_segment_ptr 1
		.amdhsa_user_sgpr_dispatch_id 0
		.amdhsa_user_sgpr_kernarg_preload_length 0
		.amdhsa_user_sgpr_kernarg_preload_offset 0
		.amdhsa_user_sgpr_private_segment_size 0
		.amdhsa_uses_dynamic_stack 0
		.amdhsa_enable_private_segment 0
		.amdhsa_system_sgpr_workgroup_id_x 1
		.amdhsa_system_sgpr_workgroup_id_y 0
		.amdhsa_system_sgpr_workgroup_id_z 0
		.amdhsa_system_sgpr_workgroup_info 0
		.amdhsa_system_vgpr_workitem_id 0
		.amdhsa_next_free_vgpr 240
		.amdhsa_next_free_sgpr 96
		.amdhsa_accum_offset 240
		.amdhsa_reserve_vcc 1
		.amdhsa_float_round_mode_32 0
		.amdhsa_float_round_mode_16_64 0
		.amdhsa_float_denorm_mode_32 3
		.amdhsa_float_denorm_mode_16_64 3
		.amdhsa_dx10_clamp 1
		.amdhsa_ieee_mode 1
		.amdhsa_fp16_overflow 0
		.amdhsa_tg_split 0
		.amdhsa_exception_fp_ieee_invalid_op 0
		.amdhsa_exception_fp_denorm_src 0
		.amdhsa_exception_fp_ieee_div_zero 0
		.amdhsa_exception_fp_ieee_overflow 0
		.amdhsa_exception_fp_ieee_underflow 0
		.amdhsa_exception_fp_ieee_inexact 0
		.amdhsa_exception_int_div_zero 0
	.end_amdhsa_kernel
	.text
.Lfunc_end2:
	.size	_Z7k_layerILi1EEvPKDF16_S1_PKfS3_S3_S3_S3_S3_S1_S1_S1_S1_S3_S3_PKhS5_PDF16_S6_PfS7_, .Lfunc_end2-_Z7k_layerILi1EEvPKDF16_S1_PKfS3_S3_S3_S3_S3_S1_S1_S1_S1_S3_S3_PKhS5_PDF16_S6_PfS7_
	.set _Z7k_layerILi1EEvPKDF16_S1_PKfS3_S3_S3_S3_S3_S1_S1_S1_S1_S3_S3_PKhS5_PDF16_S6_PfS7_.num_vgpr, 240
	.set _Z7k_layerILi1EEvPKDF16_S1_PKfS3_S3_S3_S3_S3_S1_S1_S1_S1_S3_S3_PKhS5_PDF16_S6_PfS7_.num_agpr, 0
	.set _Z7k_layerILi1EEvPKDF16_S1_PKfS3_S3_S3_S3_S3_S1_S1_S1_S1_S3_S3_PKhS5_PDF16_S6_PfS7_.numbered_sgpr, 28
	.set _Z7k_layerILi1EEvPKDF16_S1_PKfS3_S3_S3_S3_S3_S1_S1_S1_S1_S3_S3_PKhS5_PDF16_S6_PfS7_.num_named_barrier, 0
	.set _Z7k_layerILi1EEvPKDF16_S1_PKfS3_S3_S3_S3_S3_S1_S1_S1_S1_S3_S3_PKhS5_PDF16_S6_PfS7_.private_seg_size, 0
	.set _Z7k_layerILi1EEvPKDF16_S1_PKfS3_S3_S3_S3_S3_S1_S1_S1_S1_S3_S3_PKhS5_PDF16_S6_PfS7_.uses_vcc, 1
	.set _Z7k_layerILi1EEvPKDF16_S1_PKfS3_S3_S3_S3_S3_S1_S1_S1_S1_S3_S3_PKhS5_PDF16_S6_PfS7_.uses_flat_scratch, 0
	.set _Z7k_layerILi1EEvPKDF16_S1_PKfS3_S3_S3_S3_S3_S1_S1_S1_S1_S3_S3_PKhS5_PDF16_S6_PfS7_.has_dyn_sized_stack, 0
	.set _Z7k_layerILi1EEvPKDF16_S1_PKfS3_S3_S3_S3_S3_S1_S1_S1_S1_S3_S3_PKhS5_PDF16_S6_PfS7_.has_recursion, 0
	.set _Z7k_layerILi1EEvPKDF16_S1_PKfS3_S3_S3_S3_S3_S1_S1_S1_S1_S3_S3_PKhS5_PDF16_S6_PfS7_.has_indirect_call, 0

	.text
	.protected	_Z7k_layerILi0EEvPKDF16_S1_PKfS3_S3_S3_S3_S3_S1_S1_S1_S1_S3_S3_PKhS5_PDF16_S6_PfS7_
	.globl	_Z7k_layerILi0EEvPKDF16_S1_PKfS3_S3_S3_S3_S3_S1_S1_S1_S1_S3_S3_PKhS5_PDF16_S6_PfS7_
	.p2align	8
	.type	_Z7k_layerILi0EEvPKDF16_S1_PKfS3_S3_S3_S3_S3_S1_S1_S1_S1_S3_S3_PKhS5_PDF16_S6_PfS7_,@function

.LBB3_17:
	s_and_b64 vcc, exec, s[2:3]
	s_cbranch_vccz .LBB3_27
	s_setprio 2
	s_load_dwordx2 s[8:9], s[0:1], 0x70
	s_load_dwordx4 s[4:7], s[0:1], 0x40
	s_load_dwordx4 s[20:23], s[0:1], 0x10
	v_mov_b32_e32 v3, 0
	v_lshlrev_b32_e32 v2, 2, v0
	s_movk_i32 s2, 0xfe00
	s_mov_b32 s3, -1
	s_waitcnt lgkmcnt(0)
	v_lshl_add_u64 v[6:7], s[22:23], 0, v[2:3]
	s_lshr_b32 s16, s15, 7
	s_movk_i32 s10, 0x80
	v_lshl_add_u64 v[6:7], v[6:7], 0, s[2:3]
	s_lshl_b32 s2, s12, 3
	v_cmp_gt_u32_e32 vcc, s10, v0
	s_or_b32 s10, s16, s2
	v_lshl_add_u64 v[4:5], s[20:21], 0, v[2:3]
	s_ashr_i32 s11, s10, 31
	v_cndmask_b32_e32 v6, v6, v4, vcc
	s_movk_i32 s17, 0x1000
	s_bfe_u32 s13, s15, 0x10006
	s_lshl_b64 s[2:3], s[10:11], 12
	v_and_b32_e32 v156, 63, v0
	v_cndmask_b32_e32 v7, v7, v5, vcc
	v_add_co_u32_e32 v20, vcc, s17, v6
	s_add_u32 s2, s8, s2
	s_nop 0
	v_addc_co_u32_e32 v21, vcc, 0, v7, vcc
	s_addc_u32 s3, s9, s3
	v_lshlrev_b32_e32 v1, 3, v156
	global_load_dword v17, v[6:7], off
	global_load_dword v16, v[6:7], off offset:512
	global_load_dword v13, v[6:7], off offset:1024
	global_load_dword v12, v[6:7], off offset:1536
	global_load_dword v9, v[6:7], off offset:2048
	global_load_dword v8, v[6:7], off offset:2560
	global_load_dword v5, v[6:7], off offset:3072
	global_load_dword v4, v[6:7], off offset:3584
	global_load_dword v19, v[20:21], off
	global_load_dword v18, v[20:21], off offset:512
	global_load_dword v15, v[20:21], off offset:1024
	global_load_dword v14, v[20:21], off offset:1536
	global_load_dword v11, v[20:21], off offset:2048
	global_load_dword v10, v[20:21], off offset:2560
	global_load_dword v7, v[20:21], off offset:3072
	global_load_dword v6, v[20:21], off offset:3584
	global_load_dwordx2 v[154:155], v1, s[2:3]
	global_load_dwordx2 v[150:151], v1, s[2:3] offset:512
	global_load_dwordx2 v[146:147], v1, s[2:3] offset:1024
	global_load_dwordx2 v[142:143], v1, s[2:3] offset:1536
	global_load_dwordx2 v[152:153], v1, s[2:3] offset:2048
	global_load_dwordx2 v[148:149], v1, s[2:3] offset:2560
	global_load_dwordx2 v[144:145], v1, s[2:3] offset:3072
	global_load_dwordx2 v[140:141], v1, s[2:3] offset:3584
	s_lshl_b32 s2, s14, 10
	s_lshl_b32 s3, s13, 9
	s_or_b32 s2, s3, s2
	v_or_b32_e32 v1, s2, v156
	v_lshlrev_b32_e32 v20, 4, v1
	v_mov_b32_e32 v21, v3
	v_lshl_add_u64 v[22:23], s[4:5], 0, v[20:21]
	v_add_co_u32_e32 v22, vcc, s17, v22
	s_movk_i32 s2, 0x7f
	s_nop 0
	v_addc_co_u32_e32 v23, vcc, 0, v23, vcc
	global_load_dwordx4 v[86:89], v[22:23], off
	global_load_dwordx4 v[78:81], v[22:23], off offset:1024
	global_load_dwordx4 v[70:73], v[22:23], off offset:2048
	global_load_dwordx4 v[66:69], v[22:23], off offset:3072
	global_load_dwordx4 v[122:125], v20, s[4:5]
	global_load_dwordx4 v[126:129], v20, s[6:7]
	global_load_dwordx4 v[114:117], v20, s[4:5] offset:1024
	global_load_dwordx4 v[118:121], v20, s[6:7] offset:1024
	global_load_dwordx4 v[106:109], v20, s[4:5] offset:2048
	global_load_dwordx4 v[110:113], v20, s[6:7] offset:2048
	global_load_dwordx4 v[98:101], v20, s[4:5] offset:3072
	global_load_dwordx4 v[102:105], v20, s[6:7] offset:3072
	v_lshl_add_u64 v[22:23], s[6:7], 0, v[20:21]
	v_add_co_u32_e32 v20, vcc, 0x1000, v22
	s_nop 1
	v_addc_co_u32_e32 v21, vcc, 0, v23, vcc
	global_load_dwordx4 v[94:97], v[20:21], off
	global_load_dwordx4 v[90:93], v[20:21], off offset:1024
	global_load_dwordx4 v[82:85], v[20:21], off offset:2048
	global_load_dwordx4 v[74:77], v[20:21], off offset:3072
	v_cmp_lt_u32_e32 vcc, s2, v0
	v_cmp_gt_u32_e64 s[2:3], 64, v0
	s_and_saveexec_b64 s[4:5], s[2:3]
	s_cbranch_execz .LBB3_20
	s_load_dwordx2 s[2:3], s[0:1], 0x60
	v_lshl_or_b32 v1, s14, 8, v2
	v_add_u32_e32 v20, 0x1ee00, v2
	s_waitcnt lgkmcnt(0)
	global_load_dword v1, v1, s[2:3]
	s_waitcnt vmcnt(0)
	ds_write_b32 v20, v1

	.amdhsa_kernel _Z7k_layerILi0EEvPKDF16_S1_PKfS3_S3_S3_S3_S3_S1_S1_S1_S1_S3_S3_PKhS5_PDF16_S6_PfS7_
		.amdhsa_group_segment_fixed_size 126720
		.amdhsa_private_segment_fixed_size 0
		.amdhsa_kernarg_size 160
		.amdhsa_user_sgpr_count 2
		.amdhsa_user_sgpr_dispatch_ptr 0
		.amdhsa_user_sgpr_queue_ptr 0
		.amdhsa_user_sgpr_kernarg_segment_ptr 1
		.amdhsa_user_sgpr_dispatch_id 0
		.amdhsa_user_sgpr_kernarg_preload_length 0
		.amdhsa_user_sgpr_kernarg_preload_offset 0
		.amdhsa_user_sgpr_private_segment_size 0
		.amdhsa_uses_dynamic_stack 0
		.amdhsa_enable_private_segment 0
		.amdhsa_system_sgpr_workgroup_id_x 1
		.amdhsa_system_sgpr_workgroup_id_y 0
		.amdhsa_system_sgpr_workgroup_id_z 0
		.amdhsa_system_sgpr_workgroup_info 0
		.amdhsa_system_vgpr_workitem_id 0
		.amdhsa_next_free_vgpr 240
		.amdhsa_next_free_sgpr 96
		.amdhsa_accum_offset 240
		.amdhsa_reserve_vcc 1
		.amdhsa_float_round_mode_32 0
		.amdhsa_float_round_mode_16_64 0
		.amdhsa_float_denorm_mode_32 3
		.amdhsa_float_denorm_mode_16_64 3
		.amdhsa_dx10_clamp 1
		.amdhsa_ieee_mode 1
		.amdhsa_fp16_overflow 0
		.amdhsa_tg_split 0
		.amdhsa_exception_fp_ieee_invalid_op 0
		.amdhsa_exception_fp_denorm_src 0
		.amdhsa_exception_fp_ieee_div_zero 0
		.amdhsa_exception_fp_ieee_overflow 0
		.amdhsa_exception_fp_ieee_underflow 0
		.amdhsa_exception_fp_ieee_inexact 0
		.amdhsa_exception_int_div_zero 0
	.end_amdhsa_kernel
	.text
.Lfunc_end3:
	.size	_Z7k_layerILi0EEvPKDF16_S1_PKfS3_S3_S3_S3_S3_S1_S1_S1_S1_S3_S3_PKhS5_PDF16_S6_PfS7_, .Lfunc_end3-_Z7k_layerILi0EEvPKDF16_S1_PKfS3_S3_S3_S3_S3_S1_S1_S1_S1_S3_S3_PKhS5_PDF16_S6_PfS7_
	.set _Z7k_layerILi0EEvPKDF16_S1_PKfS3_S3_S3_S3_S3_S1_S1_S1_S1_S3_S3_PKhS5_PDF16_S6_PfS7_.num_vgpr, 240
	.set _Z7k_layerILi0EEvPKDF16_S1_PKfS3_S3_S3_S3_S3_S1_S1_S1_S1_S3_S3_PKhS5_PDF16_S6_PfS7_.num_agpr, 0
	.set _Z7k_layerILi0EEvPKDF16_S1_PKfS3_S3_S3_S3_S3_S1_S1_S1_S1_S3_S3_PKhS5_PDF16_S6_PfS7_.numbered_sgpr, 28
	.set _Z7k_layerILi0EEvPKDF16_S1_PKfS3_S3_S3_S3_S3_S1_S1_S1_S1_S3_S3_PKhS5_PDF16_S6_PfS7_.num_named_barrier, 0
	.set _Z7k_layerILi0EEvPKDF16_S1_PKfS3_S3_S3_S3_S3_S1_S1_S1_S1_S3_S3_PKhS5_PDF16_S6_PfS7_.private_seg_size, 0
	.set _Z7k_layerILi0EEvPKDF16_S1_PKfS3_S3_S3_S3_S3_S1_S1_S1_S1_S3_S3_PKhS5_PDF16_S6_PfS7_.uses_vcc, 1
	.set _Z7k_layerILi0EEvPKDF16_S1_PKfS3_S3_S3_S3_S3_S1_S1_S1_S1_S3_S3_PKhS5_PDF16_S6_PfS7_.uses_flat_scratch, 0
	.set _Z7k_layerILi0EEvPKDF16_S1_PKfS3_S3_S3_S3_S3_S1_S1_S1_S1_S3_S3_PKhS5_PDF16_S6_PfS7_.has_dyn_sized_stack, 0
	.set _Z7k_layerILi0EEvPKDF16_S1_PKfS3_S3_S3_S3_S3_S1_S1_S1_S1_S3_S3_PKhS5_PDF16_S6_PfS7_.has_recursion, 0
	.set _Z7k_layerILi0EEvPKDF16_S1_PKfS3_S3_S3_S3_S3_S1_S1_S1_S1_S3_S3_PKhS5_PDF16_S6_PfS7_.has_indirect_call, 0
